# LN2: rolling prefetch - next trip's row-q loads issued right after row q's block (row 0 data in fresh registers), first trip's loads before the loop
# baseline (speedup 1.0000x reference)
; __device__ __forceinline__ void ph_ln2(const Params& p, int l, LAS unsigned char* lds, const int wvid) {
;     ...
;     const LnPar ln2 = ln_par(p.in[I_LN2G] + l * D, p.in[I_LN2B] + l * D, lane);
;     int sl0 = 0, sl1 = 0; { const int myr = gw + lane * NGW; if (myr < T) { const int2 ee = *(const int2*)(TE + 2 * myr), pp = *(const int2*)(TP + 2 * myr); sl0 = tab[17 + ee.x] + pp.x; sl1 = tab[17 + ee.y] + pp.y; } }
;     int k = 0;
;     for (int r = gw; r < T; r += 4 * NGW, k += 4) {
;         u32x2 hv[4][4], av[4][4], cv[4][4]; bool on[4];
; #pragma unroll
;         for (int q = 0; q < 4; ++q) { const int rr = r + q * NGW; const int t = rr % LT; on[q] = rr < T && !(l == NLAYER - 1 && t < NMETA);
;             const int rc = rr < T ? rr : gw; const int s0 = __builtin_amdgcn_readlane(sl0, k + q), s1 = __builtin_amdgcn_readlane(sl1, k + q);
; #pragma unroll
;             for (int j = 0; j < 4; ++j) { hv[q][j] = *(const u32x2*)(HB + (size_t)rc * D + 4 * lane + 256 * j); av[q][j] = *(const u32x2*)(Y2 + (size_t)s0 * D + 4 * lane + 256 * j); cv[q][j] = *(const u32x2*)(Y2 + (size_t)s1 * D + 4 * lane + 256 * j); } }
.LBB0_1634:
	s_or_b64 exec, exec, s[0:1]
	s_mov_b32 s0, 0x8080
	v_cmp_gt_i32_e32 vcc, s0, v50
	s_and_saveexec_b64 s[0:1], vcc
	s_cbranch_execz .LBB0_1663
	v_lshlrev_b32_e32 v149, 2, v0
	v_lshlrev_b32_e32 v0, 1, v149
	v_lshl_add_u64 v[34:35], s[4:5], 0, v[0:1]
	s_mov_b64 s[4:5], 0x10000
	v_lshl_add_u64 v[52:53], v[34:35], 0, s[4:5]
	s_mov_b64 s[4:5], 0x8110000
	v_lshl_add_u64 v[54:55], v[34:35], 0, s[4:5]
	s_mov_b32 s8, 0
	s_mov_b64 s[4:5], 0
	v_mov_b32_e32 v56, v50
	s_nop 0
	v_readfirstlane_b32 s22, v50
	v_readlane_b32 s42, v254, 52
	v_readlane_b32 s43, v254, 53
	s_mul_i32 s32, s76, 24
	s_mov_b32 s62, 0
	s_nop 1
	s_mov_b32 s40, s22
	s_mov_b32 s47, s22
	s_cmp_lt_i32 s47, 0x8080
	s_cselect_b32 s48, s47, s40
	s_add_i32 s54, s62, 0
	v_readlane_b32 s50, v51, s54
	v_readlane_b32 s52, v148, s54
	s_ashr_i32 s49, s48, 31
	s_lshl_b64 s[48:49], s[48:49], 11
	s_ashr_i32 s51, s50, 31
	s_lshl_b64 s[50:51], s[50:51], 11
	s_ashr_i32 s53, s52, 31
	s_lshl_b64 s[52:53], s[52:53], 11
	v_lshl_add_u64 v[246:247], v[52:53], 0, s[48:49]
	v_lshl_add_u64 v[234:235], v[54:55], 0, s[50:51]
	v_lshl_add_u64 v[236:237], v[54:55], 0, s[52:53]
	global_load_dwordx2 v[194:195], v[246:247], off
	global_load_dwordx2 v[196:197], v[246:247], off offset:512
	global_load_dwordx2 v[198:199], v[246:247], off offset:1024
	global_load_dwordx2 v[200:201], v[246:247], off offset:1536
	global_load_dwordx2 v[202:203], v[234:235], off
	global_load_dwordx2 v[206:207], v[234:235], off offset:512
	global_load_dwordx2 v[208:209], v[234:235], off offset:1024
	global_load_dwordx2 v[210:211], v[234:235], off offset:1536
	global_load_dwordx2 v[212:213], v[236:237], off
	global_load_dwordx2 v[184:185], v[236:237], off offset:512
	global_load_dwordx2 v[186:187], v[236:237], off offset:1024
	global_load_dwordx2 v[188:189], v[236:237], off offset:1536
	s_add_i32 s47, s22, s80
	s_cmp_lt_i32 s47, 0x8080
	s_cselect_b32 s48, s47, s40
	s_add_i32 s54, s62, 1
	v_readlane_b32 s50, v51, s54
	v_readlane_b32 s52, v148, s54
	s_ashr_i32 s49, s48, 31
	s_lshl_b64 s[48:49], s[48:49], 11
	s_ashr_i32 s51, s50, 31
	s_lshl_b64 s[50:51], s[50:51], 11
	s_ashr_i32 s53, s52, 31
	s_lshl_b64 s[52:53], s[52:53], 11
	v_lshl_add_u64 v[232:233], v[52:53], 0, s[48:49]
	v_lshl_add_u64 v[234:235], v[54:55], 0, s[50:51]
	v_lshl_add_u64 v[236:237], v[54:55], 0, s[52:53]
	global_load_dwordx2 v[132:133], v[232:233], off
	global_load_dwordx2 v[126:127], v[232:233], off offset:512
	global_load_dwordx2 v[120:121], v[232:233], off offset:1024
	global_load_dwordx2 v[114:115], v[232:233], off offset:1536
	global_load_dwordx2 v[136:137], v[234:235], off
	global_load_dwordx2 v[130:131], v[234:235], off offset:512
	global_load_dwordx2 v[124:125], v[234:235], off offset:1024
	global_load_dwordx2 v[116:117], v[234:235], off offset:1536
	global_load_dwordx2 v[134:135], v[236:237], off
	global_load_dwordx2 v[128:129], v[236:237], off offset:512
	global_load_dwordx2 v[122:123], v[236:237], off offset:1024
	global_load_dwordx2 v[112:113], v[236:237], off offset:1536
	s_add_i32 s47, s22, s21
	s_cmp_lt_i32 s47, 0x8080
	s_cselect_b32 s48, s47, s40
	s_add_i32 s54, s62, 2
	v_readlane_b32 s50, v51, s54
	v_readlane_b32 s52, v148, s54
	s_ashr_i32 s49, s48, 31
	s_lshl_b64 s[48:49], s[48:49], 11
	s_ashr_i32 s51, s50, 31
	s_lshl_b64 s[50:51], s[50:51], 11
	s_ashr_i32 s53, s52, 31
	s_lshl_b64 s[52:53], s[52:53], 11
	v_lshl_add_u64 v[232:233], v[52:53], 0, s[48:49]
	v_lshl_add_u64 v[234:235], v[54:55], 0, s[50:51]
	v_lshl_add_u64 v[236:237], v[54:55], 0, s[52:53]
	global_load_dwordx2 v[106:107], v[232:233], off
	global_load_dwordx2 v[100:101], v[232:233], off offset:512
	global_load_dwordx2 v[92:93], v[232:233], off offset:1024
	global_load_dwordx2 v[88:89], v[232:233], off offset:1536
	global_load_dwordx2 v[110:111], v[234:235], off
	global_load_dwordx2 v[104:105], v[234:235], off offset:512
	global_load_dwordx2 v[96:97], v[234:235], off offset:1024
	global_load_dwordx2 v[90:91], v[234:235], off offset:1536
	global_load_dwordx2 v[108:109], v[236:237], off
	global_load_dwordx2 v[102:103], v[236:237], off offset:512
	global_load_dwordx2 v[94:95], v[236:237], off offset:1024
	global_load_dwordx2 v[86:87], v[236:237], off offset:1536
	s_add_i32 s47, s22, s32
	s_cmp_lt_i32 s47, 0x8080
	s_cselect_b32 s48, s47, s40
	s_add_i32 s54, s62, 3
	v_readlane_b32 s50, v51, s54
	v_readlane_b32 s52, v148, s54
	s_ashr_i32 s49, s48, 31
	s_lshl_b64 s[48:49], s[48:49], 11
	s_ashr_i32 s51, s50, 31
	s_lshl_b64 s[50:51], s[50:51], 11
	s_ashr_i32 s53, s52, 31
	s_lshl_b64 s[52:53], s[52:53], 11
	v_lshl_add_u64 v[232:233], v[52:53], 0, s[48:49]
	v_lshl_add_u64 v[234:235], v[54:55], 0, s[50:51]
	v_lshl_add_u64 v[236:237], v[54:55], 0, s[52:53]
	global_load_dwordx2 v[80:81], v[232:233], off
	global_load_dwordx2 v[74:75], v[232:233], off offset:512
	global_load_dwordx2 v[66:67], v[232:233], off offset:1024
	global_load_dwordx2 v[62:63], v[232:233], off offset:1536
	global_load_dwordx2 v[84:85], v[234:235], off
	global_load_dwordx2 v[78:79], v[234:235], off offset:512
	global_load_dwordx2 v[70:71], v[234:235], off offset:1024
	global_load_dwordx2 v[64:65], v[234:235], off offset:1536
	global_load_dwordx2 v[82:83], v[236:237], off
	global_load_dwordx2 v[76:77], v[236:237], off offset:512
	global_load_dwordx2 v[68:69], v[236:237], off offset:1024
	global_load_dwordx2 v[60:61], v[236:237], off offset:1536
	s_branch .LBB0_1637
.LBB0_1636:
	s_or_b64 exec, exec, s[8:9]
	s_add_i32 s46, s22, s82
	s_cmp_lt_i32 s46, 0x8080
	s_cbranch_scc0 .Lln2_drain3
	s_add_i32 s47, s46, s32
	s_cmp_lt_i32 s47, 0x8080
	s_cselect_b32 s48, s47, s40
	s_add_i32 s54, s62, 7
	v_readlane_b32 s50, v51, s54
	v_readlane_b32 s52, v148, s54
	s_ashr_i32 s49, s48, 31
	s_lshl_b64 s[48:49], s[48:49], 11
	s_ashr_i32 s51, s50, 31
	s_lshl_b64 s[50:51], s[50:51], 11
	s_ashr_i32 s53, s52, 31
	s_lshl_b64 s[52:53], s[52:53], 11
	v_lshl_add_u64 v[232:233], v[52:53], 0, s[48:49]
	v_lshl_add_u64 v[234:235], v[54:55], 0, s[50:51]
	v_lshl_add_u64 v[236:237], v[54:55], 0, s[52:53]
	global_load_dwordx2 v[80:81], v[232:233], off
	global_load_dwordx2 v[74:75], v[232:233], off offset:512
	global_load_dwordx2 v[66:67], v[232:233], off offset:1024
	global_load_dwordx2 v[62:63], v[232:233], off offset:1536
	global_load_dwordx2 v[84:85], v[234:235], off
	global_load_dwordx2 v[78:79], v[234:235], off offset:512
	global_load_dwordx2 v[70:71], v[234:235], off offset:1024
	global_load_dwordx2 v[64:65], v[234:235], off offset:1536
	global_load_dwordx2 v[82:83], v[236:237], off
	global_load_dwordx2 v[76:77], v[236:237], off offset:512
	global_load_dwordx2 v[68:69], v[236:237], off offset:1024
	global_load_dwordx2 v[60:61], v[236:237], off offset:1536
	s_branch .Lln2_next3

; __device__ __forceinline__ float bflo(unsigned w) { return __uint_as_float(w << 16); }
; __device__ __forceinline__ float bfhi(unsigned w) { return __uint_as_float(w & 0xFFFF0000u); }
; __device__ __forceinline__ void ph_ln2(const Params& p, int l, LAS unsigned char* lds, const int wvid) {
;     ...
;     for (int r = gw; r < T; r += 4 * NGW, k += 4) {
;         u32x2 hv[4][4], av[4][4], cv[4][4]; bool on[4];
; #pragma unroll
;         for (int q = 0; q < 4; ++q) { const int rr = r + q * NGW; const int t = rr % LT; on[q] = rr < T && !(l == NLAYER - 1 && t < NMETA);
;             const int rc = rr < T ? rr : gw; const int s0 = __builtin_amdgcn_readlane(sl0, k + q), s1 = __builtin_amdgcn_readlane(sl1, k + q);
; #pragma unroll
;             for (int j = 0; j < 4; ++j) { hv[q][j] = *(const u32x2*)(HB + (size_t)rc * D + 4 * lane + 256 * j); av[q][j] = *(const u32x2*)(Y2 + (size_t)s0 * D + 4 * lane + 256 * j); cv[q][j] = *(const u32x2*)(Y2 + (size_t)s1 * D + 4 * lane + 256 * j); } }
; #pragma unroll
;         for (int q = 0; q < 4; ++q) { const int rr = r + q * NGW; if (!on[q]) continue; const int b = rr / LT, t = rr % LT;
;             f32x4 v[4];
; #pragma unroll
;             for (int j = 0; j < 4; ++j) { const u32x2 h = hv[q][j], a = av[q][j], c = cv[q][j];
;                 v[j][0] = ALPHA * bflo(h.x) + bflo(a.x) + bflo(c.x); v[j][1] = ALPHA * bfhi(h.x) + bfhi(a.x) + bfhi(c.x); v[j][2] = ALPHA * bflo(h.y) + bflo(a.y) + bflo(c.y); v[j][3] = ALPHA * bfhi(h.y) + bfhi(a.y) + bfhi(c.y); }
;             ln_affine(v, ln2);
.Lln2_next3:
	v_add_u32_e32 v56, s82, v56
	s_mov_b32 s6, 0x807f
	v_cmp_lt_i32_e32 vcc, s6, v56
	s_add_i32 s62, s62, 4
	s_add_i32 s22, s22, s82
	s_or_b64 s[4:5], vcc, s[4:5]
	s_andn2_b64 exec, exec, s[4:5]
	s_cbranch_execz .LBB0_1663
.LBB0_1637:
	s_mov_b32 s16, 0x7f807f81
	v_mul_hi_i32 v0, v56, s16
	v_lshrrev_b32_e32 v57, 31, v0
	v_ashrrev_i32_e32 v0, 11, v0
	v_add_u32_e32 v138, v0, v57
	v_mul_i32_i24_e32 v0, 0x1010, v138
	v_sub_u32_e32 v0, v56, v0
	v_readlane_b32 s16, v254, 52
	v_cmp_lt_i32_e32 vcc, 15, v0
	v_readlane_b32 s17, v254, 53
	s_or_b64 s[18:19], s[16:17], vcc
	s_and_saveexec_b64 s[16:17], s[18:19]
	s_cbranch_execz .LBB0_1648
	s_waitcnt vmcnt(47)
	v_lshlrev_b32_e32 v150, 16, v194
	v_and_b32_e32 v151, 0xffff0000, v194
	s_waitcnt vmcnt(43)
	v_lshlrev_b32_e32 v152, 16, v202
	v_and_b32_e32 v153, 0xffff0000, v202
	v_lshlrev_b32_e32 v142, 16, v195
	v_and_b32_e32 v143, 0xffff0000, v195
	v_lshlrev_b32_e32 v146, 16, v203
	v_and_b32_e32 v147, 0xffff0000, v203
	v_pk_fma_f32 v[150:151], v[150:151], s[88:89], v[152:153] op_sel_hi:[1,0,1]
	s_waitcnt vmcnt(39)
	v_lshlrev_b32_e32 v152, 16, v212
	v_and_b32_e32 v153, 0xffff0000, v212
	v_pk_fma_f32 v[142:143], v[142:143], s[88:89], v[146:147] op_sel_hi:[1,0,1]
	v_lshlrev_b32_e32 v144, 16, v213
	v_and_b32_e32 v145, 0xffff0000, v213
	v_pk_add_f32 v[142:143], v[142:143], v[144:145]
	v_lshlrev_b32_e32 v144, 16, v196
	v_and_b32_e32 v145, 0xffff0000, v196
	v_lshlrev_b32_e32 v146, 16, v206
	v_and_b32_e32 v147, 0xffff0000, v206
	v_lshlrev_b32_e32 v46, 16, v197
	v_and_b32_e32 v47, 0xffff0000, v197
	v_lshlrev_b32_e32 v140, 16, v207
	v_and_b32_e32 v141, 0xffff0000, v207
	v_pk_fma_f32 v[144:145], v[144:145], s[88:89], v[146:147] op_sel_hi:[1,0,1]
	s_waitcnt vmcnt(38)
	v_lshlrev_b32_e32 v146, 16, v184
	v_and_b32_e32 v147, 0xffff0000, v184
	v_pk_fma_f32 v[46:47], v[46:47], s[88:89], v[140:141] op_sel_hi:[1,0,1]
	v_lshlrev_b32_e32 v48, 16, v185
	v_and_b32_e32 v49, 0xffff0000, v185
	v_pk_add_f32 v[140:141], v[46:47], v[48:49]
	v_lshlrev_b32_e32 v46, 16, v198
	v_and_b32_e32 v47, 0xffff0000, v198
	v_lshlrev_b32_e32 v48, 16, v208
	v_and_b32_e32 v49, 0xffff0000, v208
	v_lshlrev_b32_e32 v40, 16, v199
	v_and_b32_e32 v41, 0xffff0000, v199
	v_lshlrev_b32_e32 v44, 16, v209
	v_and_b32_e32 v45, 0xffff0000, v209
	v_pk_fma_f32 v[46:47], v[46:47], s[88:89], v[48:49] op_sel_hi:[1,0,1]
	s_waitcnt vmcnt(37)
	v_lshlrev_b32_e32 v48, 16, v186
	v_and_b32_e32 v49, 0xffff0000, v186
	v_pk_fma_f32 v[40:41], v[40:41], s[88:89], v[44:45] op_sel_hi:[1,0,1]
	v_lshlrev_b32_e32 v42, 16, v187
	v_and_b32_e32 v43, 0xffff0000, v187
	v_pk_add_f32 v[40:41], v[40:41], v[42:43]
	v_lshlrev_b32_e32 v42, 16, v200
	v_and_b32_e32 v43, 0xffff0000, v200
	v_lshlrev_b32_e32 v44, 16, v210
	v_and_b32_e32 v45, 0xffff0000, v210
	v_lshlrev_b32_e32 v36, 16, v201
	v_and_b32_e32 v37, 0xffff0000, v201
	v_lshlrev_b32_e32 v38, 16, v211
	v_and_b32_e32 v39, 0xffff0000, v211
	v_pk_add_f32 v[150:151], v[150:151], v[152:153]
	v_pk_fma_f32 v[42:43], v[42:43], s[88:89], v[44:45] op_sel_hi:[1,0,1]
	s_waitcnt vmcnt(36)
	v_lshlrev_b32_e32 v44, 16, v188
	v_and_b32_e32 v45, 0xffff0000, v188
	v_pk_fma_f32 v[36:37], v[36:37], s[88:89], v[38:39] op_sel_hi:[1,0,1]
	v_lshlrev_b32_e32 v34, 16, v189
	v_and_b32_e32 v35, 0xffff0000, v189
	v_pk_add_f32 v[144:145], v[144:145], v[146:147]
	v_pk_add_f32 v[38:39], v[36:37], v[34:35]
	v_mov_b32_e32 v34, v150
	v_mov_b32_e32 v35, v142
	v_mov_b32_e32 v36, v151
	v_mov_b32_e32 v37, v143
	v_pk_add_f32 v[152:153], v[42:43], v[44:45]
	v_pk_add_f32 v[34:35], v[34:35], v[36:37]
	v_mov_b32_e32 v36, v144
	v_mov_b32_e32 v37, v140
	v_mov_b32_e32 v42, v145
	v_mov_b32_e32 v43, v141
	v_pk_add_f32 v[146:147], v[46:47], v[48:49]
	v_pk_add_f32 v[36:37], v[36:37], v[42:43]
	v_add_f32_e32 v34, v34, v35
	v_pk_add_f32 v[36:37], v[36:37], v[36:37] op_sel:[0,1] op_sel_hi:[1,0]
	v_pk_add_f32 v[42:43], v[146:147], v[146:147] op_sel:[0,1] op_sel_hi:[1,0]
	v_pk_add_f32 v[44:45], v[40:41], v[40:41] op_sel:[0,1] op_sel_hi:[1,0]
	v_add_f32_e32 v34, 0, v34
	v_mov_b32_e32 v35, v152
	v_mov_b32_e32 v37, v153
	v_mov_b32_e32 v43, v38
	v_mov_b32_e32 v45, v39
	v_pk_add_f32 v[34:35], v[34:35], v[36:37]
	v_pk_add_f32 v[36:37], v[42:43], v[44:45]
	s_nop 0
	v_pk_add_f32 v[34:35], v[34:35], v[36:37]
	s_nop 0
	v_add_f32_e32 v34, v34, v35
	v_mov_b32_e32 v35, v1
	s_nop 0
	v_add_f32_dpp v34, v34, v34 quad_perm:[1,0,3,2] row_mask:0xf bank_mask:0xf bound_ctrl:1
	s_nop 1
	v_add_f32_dpp v34, v34, v34 quad_perm:[2,3,0,1] row_mask:0xf bank_mask:0xf bound_ctrl:1
	s_nop 1
	v_add_f32_dpp v34, v34, v34 row_half_mirror row_mask:0xf bank_mask:0xf bound_ctrl:1
	s_nop 1
	v_add_f32_dpp v34, v34, v34 row_mirror row_mask:0xf bank_mask:0xf bound_ctrl:1
	s_nop 1
	v_mov_b32_dpp v35, v34 row_bcast:15 row_mask:0xa bank_mask:0xf
	v_add_f32_e32 v34, v34, v35
	v_mov_b32_e32 v35, v1
	s_nop 1
	v_mov_b32_dpp v35, v34 row_bcast:31 row_mask:0xc bank_mask:0xf
	v_add_f32_e32 v34, v34, v35
	s_nop 0
	v_readlane_b32 s18, v34, 63
	s_nop 1
	v_fma_f32 v151, s18, v220, v151
	v_fmac_f32_e32 v150, s18, v220
	v_fma_f32 v143, s18, v220, v143
	v_fmac_f32_e32 v142, s18, v220
	v_pk_mul_f32 v[34:35], v[142:143], v[142:143]
	v_pk_mul_f32 v[36:37], v[150:151], v[150:151]
	v_fma_f32 v145, s18, v220, v145
	v_pk_mov_b32 v[42:43], v[36:37], v[34:35] op_sel:[1,0]
	v_mov_b32_e32 v37, v35
	v_pk_add_f32 v[34:35], v[42:43], v[36:37]
	v_fmac_f32_e32 v144, s18, v220
	v_fma_f32 v141, s18, v220, v141
	v_fmac_f32_e32 v140, s18, v220
	v_pk_add_f32 v[34:35], v[34:35], v[34:35] op_sel_hi:[0,1]
	v_pk_mul_f32 v[36:37], v[140:141], v[140:141]
	v_pk_mul_f32 v[42:43], v[144:145], v[144:145]
	v_fmac_f32_e32 v146, s18, v220
	v_pk_mov_b32 v[44:45], v[42:43], v[36:37] op_sel:[1,0]
; __device__ __forceinline__ float frsq(float x) { return __builtin_amdgcn_rsqf(x); }
; __device__ __forceinline__ void ln_affine(f32x4 (&v)[4], const LnPar& q) {
;     float s = 0.f;
; #pragma unroll
;     for (int j = 0; j < 4; ++j) s += (v[j][0] + v[j][1]) + (v[j][2] + v[j][3]);
;     const float mean = wave_sum(s) * (1.f / D); float s2 = 0.f;
; #pragma unroll
;     for (int j = 0; j < 4; ++j) { v[j] = v[j] - mean; s2 += (v[j][0] * v[j][0] + v[j][1] * v[j][1]) + (v[j][2] * v[j][2] + v[j][3] * v[j][3]); }
;     const float rstd = frsq(wave_sum(s2) * (1.f / D) + 1e-5f);
; #pragma unroll
;     for (int j = 0; j < 4; ++j) v[j] = v[j] * rstd * q.g[j] + q.b[j];
; }
; __device__ __forceinline__ void ph_ln2(const Params& p, int l, LAS unsigned char* lds, const int wvid) {
;     ...
;             ln_affine(v, ln2);
;             if (l == NLAYER - 1) { float* o = p.out + ((size_t)b * SEQ + (t - NMETA)) * D;
; #pragma unroll
;                 for (int j = 0; j < 4; ++j) *(f32x4*)(o + 4 * lane + 256 * j) = v[j]; }
;             else store_row_bf16(HB + (size_t)rr * D, v, lane); }
	v_mov_b32_e32 v43, v37
	v_fma_f32 v147, s18, v220, v147
	v_fmac_f32_e32 v40, s18, v220
	v_mul_f32_e32 v34, v146, v146
	v_pk_add_f32 v[36:37], v[44:45], v[42:43]
	v_fma_f32 v41, s18, v220, v41
	v_pk_fma_f32 v[42:43], v[146:147], v[146:147], v[34:35] op_sel_hi:[1,1,0]
	v_mul_f32_e32 v34, v40, v40
	v_pk_add_f32 v[36:37], v[36:37], v[36:37] op_sel_hi:[0,1]
	v_pk_fma_f32 v[44:45], v[40:41], v[40:41], v[34:35] op_sel_hi:[1,1,0]
	v_fma_f32 v39, s18, v220, v39
	v_fmac_f32_e32 v38, s18, v220
	v_fma_f32 v153, s18, v220, v153
	v_fmac_f32_e32 v152, s18, v220
	v_mul_f32_e32 v42, v152, v152
	v_mul_f32_e32 v44, v153, v153
	v_mul_f32_e32 v34, v38, v38
	v_mul_f32_e32 v36, v39, v39
	v_pk_add_f32 v[42:43], v[42:43], v[44:45]
	v_pk_add_f32 v[34:35], v[34:35], v[36:37]
	s_nop 0
	v_pk_add_f32 v[34:35], v[42:43], v[34:35]
	s_nop 0
	v_add_f32_e32 v34, v34, v35
	v_mov_b32_e32 v35, v1
	s_nop 0
	v_add_f32_dpp v34, v34, v34 quad_perm:[1,0,3,2] row_mask:0xf bank_mask:0xf bound_ctrl:1
	s_nop 1
	v_add_f32_dpp v34, v34, v34 quad_perm:[2,3,0,1] row_mask:0xf bank_mask:0xf bound_ctrl:1
	s_nop 1
	v_add_f32_dpp v34, v34, v34 row_half_mirror row_mask:0xf bank_mask:0xf bound_ctrl:1
	s_nop 1
	v_add_f32_dpp v34, v34, v34 row_mirror row_mask:0xf bank_mask:0xf bound_ctrl:1
	s_nop 1
	v_mov_b32_dpp v35, v34 row_bcast:15 row_mask:0xa bank_mask:0xf
	v_add_f32_e32 v34, v34, v35
	v_mov_b32_e32 v35, v1
	s_nop 1
	v_mov_b32_dpp v35, v34 row_bcast:31 row_mask:0xc bank_mask:0xf
	v_add_f32_e32 v34, v34, v35
	s_nop 0
	v_readlane_b32 s18, v34, 63
	s_nop 1
	v_fma_f32 v34, s18, v221, v204
	v_rsq_f32_e32 v154, v34
	v_readlane_b32 s18, v255, 10
	v_readlane_b32 s19, v255, 11
	s_andn2_b64 vcc, exec, s[18:19]
	v_pk_mul_f32 v[34:35], v[150:151], v[154:155] op_sel_hi:[1,0]
	v_pk_mul_f32 v[36:37], v[142:143], v[154:155] op_sel_hi:[1,0]
	v_pk_fma_f32 v[46:47], v[2:3], v[34:35], v[6:7]
	v_pk_fma_f32 v[48:49], v[4:5], v[36:37], v[8:9]
	v_pk_mul_f32 v[34:35], v[144:145], v[154:155] op_sel_hi:[1,0]
	v_pk_mul_f32 v[36:37], v[140:141], v[154:155] op_sel_hi:[1,0]
	v_pk_fma_f32 v[42:43], v[10:11], v[34:35], v[14:15]
	v_pk_fma_f32 v[44:45], v[12:13], v[36:37], v[16:17]
	v_pk_mul_f32 v[34:35], v[146:147], v[154:155] op_sel_hi:[1,0]
	v_pk_mul_f32 v[36:37], v[40:41], v[154:155] op_sel_hi:[1,0]
	v_pk_mul_f32 v[140:141], v[152:153], v[154:155] op_sel_hi:[1,0]
	v_pk_mul_f32 v[38:39], v[38:39], v[154:155] op_sel_hi:[1,0]
	v_pk_fma_f32 v[36:37], v[20:21], v[36:37], v[24:25]
	v_pk_fma_f32 v[34:35], v[18:19], v[34:35], v[22:23]
	v_pk_fma_f32 v[40:41], v[28:29], v[38:39], v[32:33]
	v_pk_fma_f32 v[38:39], v[26:27], v[140:141], v[30:31]
	s_mov_b64 s[18:19], -1
	s_cbranch_vccnz .LBB0_1646
	v_ashrrev_i32_e32 v139, 31, v138
	v_add_u32_e32 v140, -16, v0
	v_readlane_b32 s24, v253, 0
	v_ashrrev_i32_e32 v141, 31, v140
	v_lshlrev_b64 v[138:139], 24, v[138:139]
	v_readlane_b32 s26, v253, 2
	v_readlane_b32 s27, v253, 3
	v_lshlrev_b64 v[140:141], 12, v[140:141]
	v_lshlrev_b32_e32 v0, 2, v149
	v_lshl_add_u64 v[138:139], s[26:27], 0, v[138:139]
	v_lshl_add_u64 v[138:139], v[138:139], 0, v[140:141]
	v_lshl_add_u64 v[138:139], v[138:139], 0, v[0:1]
	s_mov_b64 s[18:19], 0
	v_readlane_b32 s25, v253, 1
	global_store_dwordx4 v[138:139], v[46:49], off
	global_store_dwordx4 v[138:139], v[42:45], off offset:1024
	global_store_dwordx4 v[138:139], v[34:37], off offset:2048
	global_store_dwordx4 v[138:139], v[38:41], off offset:3072
.LBB0_1646:
	s_andn2_b64 vcc, exec, s[18:19]
	s_cbranch_vccnz .LBB0_1648
	v_bfe_u32 v0, v46, 16, 1
	v_add3_u32 v0, v46, v0, s79
	v_bfe_u32 v46, v47, 16, 1
	v_lshrrev_b32_e32 v0, 16, v0
	v_add3_u32 v46, v47, v46, s79
	v_and_or_b32 v46, v46, s89, v0
	v_bfe_u32 v0, v48, 16, 1
	v_add3_u32 v0, v48, v0, s79
	v_bfe_u32 v47, v49, 16, 1
	v_lshrrev_b32_e32 v0, 16, v0
	v_add3_u32 v47, v49, v47, s79
	v_and_or_b32 v47, v47, s89, v0
	v_bfe_u32 v0, v42, 16, 1
	v_add3_u32 v0, v42, v0, s79
	v_bfe_u32 v42, v43, 16, 1
	v_lshrrev_b32_e32 v0, 16, v0
	v_add3_u32 v42, v43, v42, s79
	v_and_or_b32 v42, v42, s89, v0
	v_bfe_u32 v0, v44, 16, 1
	v_add3_u32 v0, v44, v0, s79
	v_bfe_u32 v43, v45, 16, 1
	v_lshrrev_b32_e32 v0, 16, v0
	v_add3_u32 v43, v45, v43, s79
	v_and_or_b32 v43, v43, s89, v0
	v_bfe_u32 v0, v34, 16, 1
	v_add3_u32 v0, v34, v0, s79
	v_bfe_u32 v34, v35, 16, 1
	v_lshrrev_b32_e32 v0, 16, v0
	v_add3_u32 v34, v35, v34, s79
	v_and_or_b32 v34, v34, s89, v0
	v_bfe_u32 v0, v36, 16, 1
	v_add3_u32 v0, v36, v0, s79
	v_bfe_u32 v35, v37, 16, 1
	v_lshrrev_b32_e32 v0, 16, v0
	v_add3_u32 v35, v37, v35, s79
	v_and_or_b32 v35, v35, s89, v0
	v_bfe_u32 v0, v38, 16, 1
	global_store_dwordx2 v[246:247], v[34:35], off offset:1024
	v_add3_u32 v0, v38, v0, s79
	v_bfe_u32 v34, v39, 16, 1
	v_lshrrev_b32_e32 v0, 16, v0
	v_add3_u32 v34, v39, v34, s79
	v_and_or_b32 v34, v34, s89, v0
	v_bfe_u32 v0, v40, 16, 1
	v_add3_u32 v0, v40, v0, s79
	v_bfe_u32 v35, v41, 16, 1
	v_lshrrev_b32_e32 v0, 16, v0
	v_add3_u32 v35, v41, v35, s79
	v_and_or_b32 v35, v35, s89, v0
	global_store_dwordx2 v[246:247], v[46:47], off
	global_store_dwordx2 v[246:247], v[42:43], off offset:512
	global_store_dwordx2 v[246:247], v[34:35], off offset:1536
.LBB0_1648:
	s_or_b64 exec, exec, s[16:17]
	s_add_i32 s46, s22, s82
	s_cmp_lt_i32 s46, 0x8080
	s_cbranch_scc0 .Lln2_drain0
	s_mov_b32 s47, s46
	s_cmp_lt_i32 s47, 0x8080
	s_cselect_b32 s48, s47, s40
	s_add_i32 s54, s62, 4
	v_readlane_b32 s50, v51, s54
	v_readlane_b32 s52, v148, s54
	s_ashr_i32 s49, s48, 31
	s_lshl_b64 s[48:49], s[48:49], 11
	s_ashr_i32 s51, s50, 31
	s_lshl_b64 s[50:51], s[50:51], 11
	s_ashr_i32 s53, s52, 31
	s_lshl_b64 s[52:53], s[52:53], 11
	v_lshl_add_u64 v[246:247], v[52:53], 0, s[48:49]
	v_lshl_add_u64 v[234:235], v[54:55], 0, s[50:51]
	v_lshl_add_u64 v[236:237], v[54:55], 0, s[52:53]
	global_load_dwordx2 v[194:195], v[246:247], off
	global_load_dwordx2 v[196:197], v[246:247], off offset:512
	global_load_dwordx2 v[198:199], v[246:247], off offset:1024
	global_load_dwordx2 v[200:201], v[246:247], off offset:1536
	global_load_dwordx2 v[202:203], v[234:235], off
	global_load_dwordx2 v[206:207], v[234:235], off offset:512
	global_load_dwordx2 v[208:209], v[234:235], off offset:1024
	global_load_dwordx2 v[210:211], v[234:235], off offset:1536
	global_load_dwordx2 v[212:213], v[236:237], off
	global_load_dwordx2 v[184:185], v[236:237], off offset:512
	global_load_dwordx2 v[186:187], v[236:237], off offset:1024
	global_load_dwordx2 v[188:189], v[236:237], off offset:1536
	s_branch .Lln2_next0

; __device__ __forceinline__ float bflo(unsigned w) { return __uint_as_float(w << 16); }
; __device__ __forceinline__ float bfhi(unsigned w) { return __uint_as_float(w & 0xFFFF0000u); }
; __device__ __forceinline__ void ph_ln2(const Params& p, int l, LAS unsigned char* lds, const int wvid) {
;     ...
;         for (int q = 0; q < 4; ++q) { const int rr = r + q * NGW; const int t = rr % LT; on[q] = rr < T && !(l == NLAYER - 1 && t < NMETA);
;             const int rc = rr < T ? rr : gw; const int s0 = __builtin_amdgcn_readlane(sl0, k + q), s1 = __builtin_amdgcn_readlane(sl1, k + q);
; #pragma unroll
;             for (int j = 0; j < 4; ++j) { hv[q][j] = *(const u32x2*)(HB + (size_t)rc * D + 4 * lane + 256 * j); av[q][j] = *(const u32x2*)(Y2 + (size_t)s0 * D + 4 * lane + 256 * j); cv[q][j] = *(const u32x2*)(Y2 + (size_t)s1 * D + 4 * lane + 256 * j); } }
; #pragma unroll
;         for (int q = 0; q < 4; ++q) { const int rr = r + q * NGW; if (!on[q]) continue; const int b = rr / LT, t = rr % LT;
;             f32x4 v[4];
; #pragma unroll
;             for (int j = 0; j < 4; ++j) { const u32x2 h = hv[q][j], a = av[q][j], c = cv[q][j];
;                 v[j][0] = ALPHA * bflo(h.x) + bflo(a.x) + bflo(c.x); v[j][1] = ALPHA * bfhi(h.x) + bfhi(a.x) + bfhi(c.x); v[j][2] = ALPHA * bflo(h.y) + bflo(a.y) + bflo(c.y); v[j][3] = ALPHA * bfhi(h.y) + bfhi(a.y) + bfhi(c.y); }
.Lln2_next0:
	v_add_u32_e32 v98, s80, v56
	s_add_i32 s60, s22, s80
	s_mul_hi_i32 s61, s60, 0x7f807f81
	s_lshr_b32 s55, s61, 31
	s_ashr_i32 s61, s61, 11
	s_add_i32 s61, s61, s55
	s_mul_i32 s61, s61, 0x1010
	s_sub_i32 s61, s60, s61
	s_cmp_gt_i32 s61, 15
	s_cselect_b64 s[10:11], -1, 0
	s_or_b64 s[10:11], s[10:11], s[42:43]
	s_cmp_lt_i32 s60, 0x8080
	s_cselect_b64 s[58:59], -1, 0
	s_and_b64 s[10:11], s[10:11], s[58:59]
	s_and_saveexec_b64 s[16:17], s[10:11]
	s_cbranch_execz .LBB0_1653
	s_waitcnt vmcnt(47)
	v_lshlrev_b32_e32 v34, 16, v132
	v_and_b32_e32 v35, 0xffff0000, v132
	s_waitcnt vmcnt(43)
	v_lshlrev_b32_e32 v36, 16, v136
	v_and_b32_e32 v37, 0xffff0000, v136
	v_pk_fma_f32 v[34:35], v[34:35], s[88:89], v[36:37] op_sel_hi:[1,0,1]
	s_waitcnt vmcnt(39)
	v_lshlrev_b32_e32 v36, 16, v134
	v_and_b32_e32 v37, 0xffff0000, v134
	v_pk_add_f32 v[34:35], v[34:35], v[36:37]
	v_lshlrev_b32_e32 v36, 16, v133
	v_and_b32_e32 v37, 0xffff0000, v133
	v_lshlrev_b32_e32 v38, 16, v137
	v_and_b32_e32 v39, 0xffff0000, v137
	v_pk_fma_f32 v[36:37], v[36:37], s[88:89], v[38:39] op_sel_hi:[1,0,1]
	v_lshlrev_b32_e32 v38, 16, v135
	v_and_b32_e32 v39, 0xffff0000, v135
	v_pk_add_f32 v[36:37], v[36:37], v[38:39]
	v_lshlrev_b32_e32 v38, 16, v126
	v_and_b32_e32 v39, 0xffff0000, v126
	v_lshlrev_b32_e32 v40, 16, v130
	v_and_b32_e32 v41, 0xffff0000, v130
	v_pk_fma_f32 v[38:39], v[38:39], s[88:89], v[40:41] op_sel_hi:[1,0,1]
	s_waitcnt vmcnt(38)
	v_lshlrev_b32_e32 v40, 16, v128
	v_and_b32_e32 v41, 0xffff0000, v128
	v_pk_add_f32 v[38:39], v[38:39], v[40:41]
	v_lshlrev_b32_e32 v40, 16, v127
	v_and_b32_e32 v41, 0xffff0000, v127
	v_lshlrev_b32_e32 v42, 16, v131
	v_and_b32_e32 v43, 0xffff0000, v131
	v_pk_fma_f32 v[40:41], v[40:41], s[88:89], v[42:43] op_sel_hi:[1,0,1]
	v_lshlrev_b32_e32 v42, 16, v129
	v_and_b32_e32 v43, 0xffff0000, v129
	v_pk_add_f32 v[40:41], v[40:41], v[42:43]
	v_lshlrev_b32_e32 v42, 16, v120
	v_and_b32_e32 v43, 0xffff0000, v120
	v_lshlrev_b32_e32 v44, 16, v124
	v_and_b32_e32 v45, 0xffff0000, v124
	v_pk_fma_f32 v[42:43], v[42:43], s[88:89], v[44:45] op_sel_hi:[1,0,1]
	s_waitcnt vmcnt(37)
	v_lshlrev_b32_e32 v44, 16, v122
	v_and_b32_e32 v45, 0xffff0000, v122
	v_pk_add_f32 v[118:119], v[42:43], v[44:45]
	v_lshlrev_b32_e32 v42, 16, v121
	v_and_b32_e32 v43, 0xffff0000, v121
	v_lshlrev_b32_e32 v44, 16, v125
	v_and_b32_e32 v45, 0xffff0000, v125
	v_pk_fma_f32 v[42:43], v[42:43], s[88:89], v[44:45] op_sel_hi:[1,0,1]
	v_lshlrev_b32_e32 v44, 16, v123
	v_and_b32_e32 v45, 0xffff0000, v123
	v_pk_add_f32 v[120:121], v[42:43], v[44:45]
	v_lshlrev_b32_e32 v42, 16, v114
	v_and_b32_e32 v43, 0xffff0000, v114
	v_lshlrev_b32_e32 v44, 16, v116
	v_and_b32_e32 v45, 0xffff0000, v116
	v_pk_fma_f32 v[42:43], v[42:43], s[88:89], v[44:45] op_sel_hi:[1,0,1]
	s_waitcnt vmcnt(36)
; __device__ __forceinline__ float frsq(float x) { return __builtin_amdgcn_rsqf(x); }
; __device__ __forceinline__ void ln_affine(f32x4 (&v)[4], const LnPar& q) {
;     float s = 0.f;
; #pragma unroll
;     for (int j = 0; j < 4; ++j) s += (v[j][0] + v[j][1]) + (v[j][2] + v[j][3]);
;     const float mean = wave_sum(s) * (1.f / D); float s2 = 0.f;
; #pragma unroll
;     for (int j = 0; j < 4; ++j) { v[j] = v[j] - mean; s2 += (v[j][0] * v[j][0] + v[j][1] * v[j][1]) + (v[j][2] * v[j][2] + v[j][3] * v[j][3]); }
;     const float rstd = frsq(wave_sum(s2) * (1.f / D) + 1e-5f);
; #pragma unroll
;     for (int j = 0; j < 4; ++j) v[j] = v[j] * rstd * q.g[j] + q.b[j];
; }
; __device__ __forceinline__ void ph_ln2(const Params& p, int l, LAS unsigned char* lds, const int wvid) {
;     ...
;             ln_affine(v, ln2);
;             if (l == NLAYER - 1) { float* o = p.out + ((size_t)b * SEQ + (t - NMETA)) * D;
; #pragma unroll
;                 for (int j = 0; j < 4; ++j) *(f32x4*)(o + 4 * lane + 256 * j) = v[j]; }
	v_lshlrev_b32_e32 v44, 16, v112
	v_and_b32_e32 v45, 0xffff0000, v112
	v_pk_add_f32 v[122:123], v[42:43], v[44:45]
	v_lshlrev_b32_e32 v42, 16, v115
	v_and_b32_e32 v43, 0xffff0000, v115
	v_lshlrev_b32_e32 v44, 16, v117
	v_and_b32_e32 v45, 0xffff0000, v117
	v_pk_fma_f32 v[42:43], v[42:43], s[88:89], v[44:45] op_sel_hi:[1,0,1]
	v_lshlrev_b32_e32 v44, 16, v113
	v_and_b32_e32 v45, 0xffff0000, v113
	v_pk_add_f32 v[112:113], v[42:43], v[44:45]
	v_mov_b32_e32 v42, v34
	v_mov_b32_e32 v43, v36
	v_mov_b32_e32 v44, v35
	v_mov_b32_e32 v45, v37
	v_pk_add_f32 v[42:43], v[42:43], v[44:45]
	v_mov_b32_e32 v44, v38
	v_mov_b32_e32 v45, v40
	v_mov_b32_e32 v46, v39
	v_mov_b32_e32 v47, v41
	v_pk_add_f32 v[44:45], v[44:45], v[46:47]
	v_add_f32_e32 v0, v42, v43
	v_pk_add_f32 v[44:45], v[44:45], v[44:45] op_sel:[0,1] op_sel_hi:[1,0]
	v_pk_add_f32 v[46:47], v[118:119], v[118:119] op_sel:[0,1] op_sel_hi:[1,0]
	v_pk_add_f32 v[48:49], v[120:121], v[120:121] op_sel:[0,1] op_sel_hi:[1,0]
	v_add_f32_e32 v42, 0, v0
	v_mov_b32_e32 v43, v122
	v_mov_b32_e32 v45, v123
	v_mov_b32_e32 v47, v112
	v_mov_b32_e32 v49, v113
	v_pk_add_f32 v[42:43], v[42:43], v[44:45]
	v_pk_add_f32 v[44:45], v[46:47], v[48:49]
	s_nop 0
	v_pk_add_f32 v[42:43], v[42:43], v[44:45]
	s_nop 0
	v_add_f32_e32 v0, v42, v43
	v_mov_b32_e32 v42, v1
	s_nop 0
	v_add_f32_dpp v0, v0, v0 quad_perm:[1,0,3,2] row_mask:0xf bank_mask:0xf bound_ctrl:1
	s_nop 1
	v_add_f32_dpp v0, v0, v0 quad_perm:[2,3,0,1] row_mask:0xf bank_mask:0xf bound_ctrl:1
	s_nop 1
	v_add_f32_dpp v0, v0, v0 row_half_mirror row_mask:0xf bank_mask:0xf bound_ctrl:1
	s_nop 1
	v_add_f32_dpp v0, v0, v0 row_mirror row_mask:0xf bank_mask:0xf bound_ctrl:1
	s_nop 1
	v_mov_b32_dpp v42, v0 row_bcast:15 row_mask:0xa bank_mask:0xf
	v_add_f32_e32 v0, v0, v42
	v_mov_b32_e32 v42, v1
	s_nop 1
	v_mov_b32_dpp v42, v0 row_bcast:31 row_mask:0xc bank_mask:0xf
	v_add_f32_e32 v0, v0, v42
	s_nop 0
	v_readlane_b32 s10, v0, 63
	s_nop 1
	v_fma_f32 v35, s10, v220, v35
	v_fmac_f32_e32 v34, s10, v220
	v_fma_f32 v37, s10, v220, v37
	v_fmac_f32_e32 v36, s10, v220
	v_pk_mul_f32 v[42:43], v[36:37], v[36:37]
	v_pk_mul_f32 v[44:45], v[34:35], v[34:35]
	v_fma_f32 v39, s10, v220, v39
	v_pk_mov_b32 v[46:47], v[44:45], v[42:43] op_sel:[1,0]
	v_mov_b32_e32 v45, v43
	v_fmac_f32_e32 v38, s10, v220
	v_fma_f32 v41, s10, v220, v41
	v_fmac_f32_e32 v40, s10, v220
	v_pk_add_f32 v[42:43], v[46:47], v[44:45]
	v_pk_mul_f32 v[44:45], v[40:41], v[40:41]
	v_pk_mul_f32 v[46:47], v[38:39], v[38:39]
	v_fmac_f32_e32 v118, s10, v220
	v_pk_mov_b32 v[48:49], v[46:47], v[44:45] op_sel:[1,0]
	v_mov_b32_e32 v47, v45
	v_fma_f32 v119, s10, v220, v119
	v_fmac_f32_e32 v120, s10, v220
	v_mul_f32_e32 v0, v118, v118
	v_pk_add_f32 v[44:45], v[48:49], v[46:47]
	v_fma_f32 v121, s10, v220, v121
	v_pk_fma_f32 v[46:47], v[118:119], v[118:119], v[0:1] op_sel_hi:[1,1,0]
	v_mul_f32_e32 v0, v120, v120
	v_pk_add_f32 v[42:43], v[42:43], v[42:43] op_sel_hi:[0,1]
	v_pk_add_f32 v[44:45], v[44:45], v[44:45] op_sel_hi:[0,1]
	v_pk_fma_f32 v[48:49], v[120:121], v[120:121], v[0:1] op_sel_hi:[1,1,0]
	v_fma_f32 v113, s10, v220, v113
	v_fmac_f32_e32 v112, s10, v220
	v_fma_f32 v123, s10, v220, v123
	v_fmac_f32_e32 v122, s10, v220
	v_mul_f32_e32 v46, v122, v122
	v_mul_f32_e32 v48, v123, v123
	v_mul_f32_e32 v42, v112, v112
	v_mul_f32_e32 v44, v113, v113
	v_pk_add_f32 v[46:47], v[46:47], v[48:49]
	v_pk_add_f32 v[42:43], v[42:43], v[44:45]
	s_nop 0
	v_pk_add_f32 v[42:43], v[46:47], v[42:43]
	s_nop 0
	v_add_f32_e32 v0, v42, v43
	v_mov_b32_e32 v42, v1
	s_nop 0
	v_add_f32_dpp v0, v0, v0 quad_perm:[1,0,3,2] row_mask:0xf bank_mask:0xf bound_ctrl:1
	s_nop 1
	v_add_f32_dpp v0, v0, v0 quad_perm:[2,3,0,1] row_mask:0xf bank_mask:0xf bound_ctrl:1
	s_nop 1
	v_add_f32_dpp v0, v0, v0 row_half_mirror row_mask:0xf bank_mask:0xf bound_ctrl:1
	s_nop 1
	v_add_f32_dpp v0, v0, v0 row_mirror row_mask:0xf bank_mask:0xf bound_ctrl:1
	s_nop 1
	v_mov_b32_dpp v42, v0 row_bcast:15 row_mask:0xa bank_mask:0xf
	v_add_f32_e32 v0, v0, v42
	v_mov_b32_e32 v42, v1
	s_nop 1
	v_mov_b32_dpp v42, v0 row_bcast:31 row_mask:0xc bank_mask:0xf
	v_add_f32_e32 v0, v0, v42
	s_nop 0
	v_readlane_b32 s10, v0, 63
	s_nop 1
	v_fma_f32 v0, s10, v221, v204
	v_rsq_f32_e32 v0, v0
	v_readlane_b32 s10, v255, 10
	v_readlane_b32 s11, v255, 11
	s_andn2_b64 vcc, exec, s[10:11]
	v_pk_mul_f32 v[34:35], v[34:35], v[0:1] op_sel_hi:[1,0]
	v_pk_mul_f32 v[36:37], v[36:37], v[0:1] op_sel_hi:[1,0]
	v_pk_fma_f32 v[46:47], v[2:3], v[34:35], v[6:7]
	v_pk_fma_f32 v[48:49], v[4:5], v[36:37], v[8:9]
	v_pk_mul_f32 v[34:35], v[38:39], v[0:1] op_sel_hi:[1,0]
	v_pk_mul_f32 v[36:37], v[40:41], v[0:1] op_sel_hi:[1,0]
	v_pk_fma_f32 v[42:43], v[10:11], v[34:35], v[14:15]
	v_pk_fma_f32 v[44:45], v[12:13], v[36:37], v[16:17]
	v_pk_mul_f32 v[34:35], v[118:119], v[0:1] op_sel_hi:[1,0]
	v_pk_mul_f32 v[36:37], v[120:121], v[0:1] op_sel_hi:[1,0]
	v_pk_mul_f32 v[38:39], v[122:123], v[0:1] op_sel_hi:[1,0]
	v_pk_mul_f32 v[40:41], v[112:113], v[0:1] op_sel_hi:[1,0]
	v_pk_fma_f32 v[36:37], v[20:21], v[36:37], v[24:25]
	v_pk_fma_f32 v[34:35], v[18:19], v[34:35], v[22:23]
	v_pk_fma_f32 v[40:41], v[28:29], v[40:41], v[32:33]
	v_pk_fma_f32 v[38:39], v[26:27], v[38:39], v[30:31]
	s_mov_b64 s[10:11], -1
	s_cbranch_vccnz .LBB0_1651
	s_mov_b32 s10, 0x7f807f81
	v_mul_hi_i32 v0, v98, s10
	v_lshrrev_b32_e32 v57, 31, v0
	v_ashrrev_i32_e32 v0, 11, v0
	v_add_u32_e32 v112, v0, v57
	v_mul_i32_i24_e32 v0, 0x1010, v112
	v_sub_u32_e32 v114, v98, v0
	v_ashrrev_i32_e32 v113, 31, v112
	v_readlane_b32 s24, v253, 0
	v_ashrrev_i32_e32 v115, 31, v114
	v_lshlrev_b64 v[112:113], 24, v[112:113]
	v_readlane_b32 s26, v253, 2
	v_readlane_b32 s27, v253, 3
	v_lshlrev_b64 v[114:115], 12, v[114:115]
	v_lshlrev_b32_e32 v0, 2, v149
	v_lshl_add_u64 v[112:113], s[26:27], 0, v[112:113]
	v_lshl_add_u64 v[112:113], v[112:113], 0, v[114:115]
	s_mov_b32 s10, 0xffff0000
	v_lshl_add_u64 v[112:113], v[112:113], 0, v[0:1]
	s_mov_b32 s11, -1
	v_lshl_add_u64 v[114:115], v[112:113], 0, s[10:11]
	v_add_co_u32_e32 v112, vcc, 0xffff0000, v112
	s_mov_b64 s[10:11], 0
	s_nop 0
	v_addc_co_u32_e32 v113, vcc, -1, v113, vcc
	v_readlane_b32 s25, v253, 1
	global_store_dwordx4 v[112:113], v[46:49], off
	global_store_dwordx4 v[114:115], v[42:45], off offset:1024
	global_store_dwordx4 v[114:115], v[34:37], off offset:2048
	global_store_dwordx4 v[114:115], v[38:41], off offset:3072

; __device__ __forceinline__ void ph_ln2(const Params& p, int l, LAS unsigned char* lds, const int wvid) {
;     ...
;     for (int r = gw; r < T; r += 4 * NGW, k += 4) {
;         u32x2 hv[4][4], av[4][4], cv[4][4]; bool on[4];
; #pragma unroll
;         for (int q = 0; q < 4; ++q) { const int rr = r + q * NGW; const int t = rr % LT; on[q] = rr < T && !(l == NLAYER - 1 && t < NMETA);
;             const int rc = rr < T ? rr : gw; const int s0 = __builtin_amdgcn_readlane(sl0, k + q), s1 = __builtin_amdgcn_readlane(sl1, k + q);
; #pragma unroll
;             for (int j = 0; j < 4; ++j) { hv[q][j] = *(const u32x2*)(HB + (size_t)rc * D + 4 * lane + 256 * j); av[q][j] = *(const u32x2*)(Y2 + (size_t)s0 * D + 4 * lane + 256 * j); cv[q][j] = *(const u32x2*)(Y2 + (size_t)s1 * D + 4 * lane + 256 * j); } }
.LBB0_1653:
	s_or_b64 exec, exec, s[16:17]
	s_add_i32 s46, s22, s82
	s_cmp_lt_i32 s46, 0x8080
	s_cbranch_scc0 .Lln2_drain1
	s_add_i32 s47, s46, s80
	s_cmp_lt_i32 s47, 0x8080
	s_cselect_b32 s48, s47, s40
	s_add_i32 s54, s62, 5
	v_readlane_b32 s50, v51, s54
	v_readlane_b32 s52, v148, s54
	s_ashr_i32 s49, s48, 31
	s_lshl_b64 s[48:49], s[48:49], 11
	s_ashr_i32 s51, s50, 31
	s_lshl_b64 s[50:51], s[50:51], 11
	s_ashr_i32 s53, s52, 31
	s_lshl_b64 s[52:53], s[52:53], 11
	v_lshl_add_u64 v[232:233], v[52:53], 0, s[48:49]
	v_lshl_add_u64 v[234:235], v[54:55], 0, s[50:51]
	v_lshl_add_u64 v[236:237], v[54:55], 0, s[52:53]
	global_load_dwordx2 v[132:133], v[232:233], off
	global_load_dwordx2 v[126:127], v[232:233], off offset:512
	global_load_dwordx2 v[120:121], v[232:233], off offset:1024
	global_load_dwordx2 v[114:115], v[232:233], off offset:1536
	global_load_dwordx2 v[136:137], v[234:235], off
	global_load_dwordx2 v[130:131], v[234:235], off offset:512
	global_load_dwordx2 v[124:125], v[234:235], off offset:1024
	global_load_dwordx2 v[116:117], v[234:235], off offset:1536
	global_load_dwordx2 v[134:135], v[236:237], off
	global_load_dwordx2 v[128:129], v[236:237], off offset:512
	global_load_dwordx2 v[122:123], v[236:237], off offset:1024
	global_load_dwordx2 v[112:113], v[236:237], off offset:1536
	s_branch .Lln2_next1

; __device__ __forceinline__ float bflo(unsigned w) { return __uint_as_float(w << 16); }
; __device__ __forceinline__ float bfhi(unsigned w) { return __uint_as_float(w & 0xFFFF0000u); }
; __device__ __forceinline__ void ph_ln2(const Params& p, int l, LAS unsigned char* lds, const int wvid) {
;     ...
;         for (int q = 0; q < 4; ++q) { const int rr = r + q * NGW; const int t = rr % LT; on[q] = rr < T && !(l == NLAYER - 1 && t < NMETA);
;             const int rc = rr < T ? rr : gw; const int s0 = __builtin_amdgcn_readlane(sl0, k + q), s1 = __builtin_amdgcn_readlane(sl1, k + q);
; #pragma unroll
;             for (int j = 0; j < 4; ++j) { hv[q][j] = *(const u32x2*)(HB + (size_t)rc * D + 4 * lane + 256 * j); av[q][j] = *(const u32x2*)(Y2 + (size_t)s0 * D + 4 * lane + 256 * j); cv[q][j] = *(const u32x2*)(Y2 + (size_t)s1 * D + 4 * lane + 256 * j); } }
; #pragma unroll
;         for (int q = 0; q < 4; ++q) { const int rr = r + q * NGW; if (!on[q]) continue; const int b = rr / LT, t = rr % LT;
;             f32x4 v[4];
; #pragma unroll
;             for (int j = 0; j < 4; ++j) { const u32x2 h = hv[q][j], a = av[q][j], c = cv[q][j];
;                 v[j][0] = ALPHA * bflo(h.x) + bflo(a.x) + bflo(c.x); v[j][1] = ALPHA * bfhi(h.x) + bfhi(a.x) + bfhi(c.x); v[j][2] = ALPHA * bflo(h.y) + bflo(a.y) + bflo(c.y); v[j][3] = ALPHA * bfhi(h.y) + bfhi(a.y) + bfhi(c.y); }
.Lln2_next1:
	v_add_u32_e32 v72, s21, v56
	s_add_i32 s60, s22, s21
	s_mul_hi_i32 s61, s60, 0x7f807f81
	s_lshr_b32 s55, s61, 31
	s_ashr_i32 s61, s61, 11
	s_add_i32 s61, s61, s55
	s_mul_i32 s61, s61, 0x1010
	s_sub_i32 s61, s60, s61
	s_cmp_gt_i32 s61, 15
	s_cselect_b64 s[8:9], -1, 0
	s_or_b64 s[8:9], s[8:9], s[42:43]
	s_cmp_lt_i32 s60, 0x8080
	s_cselect_b64 s[58:59], -1, 0
	s_and_b64 s[8:9], s[8:9], s[58:59]
	s_and_saveexec_b64 s[10:11], s[8:9]
	s_cbranch_execz .LBB0_1658
	s_waitcnt vmcnt(47)
	v_lshlrev_b32_e32 v34, 16, v106
	v_and_b32_e32 v35, 0xffff0000, v106
	s_waitcnt vmcnt(43)
	v_lshlrev_b32_e32 v36, 16, v110
	v_and_b32_e32 v37, 0xffff0000, v110
	v_pk_fma_f32 v[34:35], v[34:35], s[88:89], v[36:37] op_sel_hi:[1,0,1]
	s_waitcnt vmcnt(39)
	v_lshlrev_b32_e32 v36, 16, v108
	v_and_b32_e32 v37, 0xffff0000, v108
	v_pk_add_f32 v[34:35], v[34:35], v[36:37]
	v_lshlrev_b32_e32 v36, 16, v107
	v_and_b32_e32 v37, 0xffff0000, v107
	v_lshlrev_b32_e32 v38, 16, v111
	v_and_b32_e32 v39, 0xffff0000, v111
	v_pk_fma_f32 v[36:37], v[36:37], s[88:89], v[38:39] op_sel_hi:[1,0,1]
	v_lshlrev_b32_e32 v38, 16, v109
	v_and_b32_e32 v39, 0xffff0000, v109
	v_pk_add_f32 v[36:37], v[36:37], v[38:39]
	v_lshlrev_b32_e32 v38, 16, v100
	v_and_b32_e32 v39, 0xffff0000, v100
	v_lshlrev_b32_e32 v40, 16, v104
	v_and_b32_e32 v41, 0xffff0000, v104
	v_pk_fma_f32 v[38:39], v[38:39], s[88:89], v[40:41] op_sel_hi:[1,0,1]
	s_waitcnt vmcnt(38)
	v_lshlrev_b32_e32 v40, 16, v102
	v_and_b32_e32 v41, 0xffff0000, v102
	v_pk_add_f32 v[38:39], v[38:39], v[40:41]
	v_lshlrev_b32_e32 v40, 16, v101
	v_and_b32_e32 v41, 0xffff0000, v101
	v_lshlrev_b32_e32 v42, 16, v105
	v_and_b32_e32 v43, 0xffff0000, v105
	v_pk_fma_f32 v[40:41], v[40:41], s[88:89], v[42:43] op_sel_hi:[1,0,1]
	v_lshlrev_b32_e32 v42, 16, v103
	v_and_b32_e32 v43, 0xffff0000, v103
	v_pk_add_f32 v[40:41], v[40:41], v[42:43]
	v_lshlrev_b32_e32 v42, 16, v92
	v_and_b32_e32 v43, 0xffff0000, v92
	v_lshlrev_b32_e32 v44, 16, v96
	v_and_b32_e32 v45, 0xffff0000, v96
	v_pk_fma_f32 v[42:43], v[42:43], s[88:89], v[44:45] op_sel_hi:[1,0,1]
	s_waitcnt vmcnt(37)
	v_lshlrev_b32_e32 v44, 16, v94
	v_and_b32_e32 v45, 0xffff0000, v94
	v_pk_add_f32 v[98:99], v[42:43], v[44:45]
	v_lshlrev_b32_e32 v42, 16, v93
	v_and_b32_e32 v43, 0xffff0000, v93
	v_lshlrev_b32_e32 v44, 16, v97
	v_and_b32_e32 v45, 0xffff0000, v97
	v_pk_fma_f32 v[42:43], v[42:43], s[88:89], v[44:45] op_sel_hi:[1,0,1]
	v_lshlrev_b32_e32 v44, 16, v95
	v_and_b32_e32 v45, 0xffff0000, v95
	v_pk_add_f32 v[92:93], v[42:43], v[44:45]
	v_lshlrev_b32_e32 v42, 16, v88
	v_and_b32_e32 v43, 0xffff0000, v88
	v_lshlrev_b32_e32 v44, 16, v90
	v_and_b32_e32 v45, 0xffff0000, v90
	v_pk_fma_f32 v[42:43], v[42:43], s[88:89], v[44:45] op_sel_hi:[1,0,1]
	s_waitcnt vmcnt(36)
; __device__ __forceinline__ float frsq(float x) { return __builtin_amdgcn_rsqf(x); }
; __device__ __forceinline__ void ln_affine(f32x4 (&v)[4], const LnPar& q) {
;     float s = 0.f;
; #pragma unroll
;     for (int j = 0; j < 4; ++j) s += (v[j][0] + v[j][1]) + (v[j][2] + v[j][3]);
;     const float mean = wave_sum(s) * (1.f / D); float s2 = 0.f;
; #pragma unroll
;     for (int j = 0; j < 4; ++j) { v[j] = v[j] - mean; s2 += (v[j][0] * v[j][0] + v[j][1] * v[j][1]) + (v[j][2] * v[j][2] + v[j][3] * v[j][3]); }
;     const float rstd = frsq(wave_sum(s2) * (1.f / D) + 1e-5f);
; #pragma unroll
;     for (int j = 0; j < 4; ++j) v[j] = v[j] * rstd * q.g[j] + q.b[j];
; }
; __device__ __forceinline__ void ph_ln2(const Params& p, int l, LAS unsigned char* lds, const int wvid) {
;     ...
;             ln_affine(v, ln2);
;             if (l == NLAYER - 1) { float* o = p.out + ((size_t)b * SEQ + (t - NMETA)) * D;
; #pragma unroll
;                 for (int j = 0; j < 4; ++j) *(f32x4*)(o + 4 * lane + 256 * j) = v[j]; }
	v_lshlrev_b32_e32 v44, 16, v86
	v_and_b32_e32 v45, 0xffff0000, v86
	v_pk_add_f32 v[94:95], v[42:43], v[44:45]
	v_lshlrev_b32_e32 v42, 16, v89
	v_and_b32_e32 v43, 0xffff0000, v89
	v_lshlrev_b32_e32 v44, 16, v91
	v_and_b32_e32 v45, 0xffff0000, v91
	v_pk_fma_f32 v[42:43], v[42:43], s[88:89], v[44:45] op_sel_hi:[1,0,1]
	v_lshlrev_b32_e32 v44, 16, v87
	v_and_b32_e32 v45, 0xffff0000, v87
	v_pk_add_f32 v[86:87], v[42:43], v[44:45]
	v_mov_b32_e32 v42, v34
	v_mov_b32_e32 v43, v36
	v_mov_b32_e32 v44, v35
	v_mov_b32_e32 v45, v37
	v_pk_add_f32 v[42:43], v[42:43], v[44:45]
	v_mov_b32_e32 v44, v38
	v_mov_b32_e32 v45, v40
	v_mov_b32_e32 v46, v39
	v_mov_b32_e32 v47, v41
	v_pk_add_f32 v[44:45], v[44:45], v[46:47]
	v_add_f32_e32 v0, v42, v43
	v_pk_add_f32 v[44:45], v[44:45], v[44:45] op_sel:[0,1] op_sel_hi:[1,0]
	v_pk_add_f32 v[46:47], v[98:99], v[98:99] op_sel:[0,1] op_sel_hi:[1,0]
	v_pk_add_f32 v[48:49], v[92:93], v[92:93] op_sel:[0,1] op_sel_hi:[1,0]
	v_add_f32_e32 v42, 0, v0
	v_mov_b32_e32 v43, v94
	v_mov_b32_e32 v45, v95
	v_mov_b32_e32 v47, v86
	v_mov_b32_e32 v49, v87
	v_pk_add_f32 v[42:43], v[42:43], v[44:45]
	v_pk_add_f32 v[44:45], v[46:47], v[48:49]
	s_nop 0
	v_pk_add_f32 v[42:43], v[42:43], v[44:45]
	s_nop 0
	v_add_f32_e32 v0, v42, v43
	v_mov_b32_e32 v42, v1
	s_nop 0
	v_add_f32_dpp v0, v0, v0 quad_perm:[1,0,3,2] row_mask:0xf bank_mask:0xf bound_ctrl:1
	s_nop 1
	v_add_f32_dpp v0, v0, v0 quad_perm:[2,3,0,1] row_mask:0xf bank_mask:0xf bound_ctrl:1
	s_nop 1
	v_add_f32_dpp v0, v0, v0 row_half_mirror row_mask:0xf bank_mask:0xf bound_ctrl:1
	s_nop 1
	v_add_f32_dpp v0, v0, v0 row_mirror row_mask:0xf bank_mask:0xf bound_ctrl:1
	s_nop 1
	v_mov_b32_dpp v42, v0 row_bcast:15 row_mask:0xa bank_mask:0xf
	v_add_f32_e32 v0, v0, v42
	v_mov_b32_e32 v42, v1
	s_nop 1
	v_mov_b32_dpp v42, v0 row_bcast:31 row_mask:0xc bank_mask:0xf
	v_add_f32_e32 v0, v0, v42
	s_nop 0
	v_readlane_b32 s8, v0, 63
	s_nop 1
	v_fma_f32 v35, s8, v220, v35
	v_fmac_f32_e32 v34, s8, v220
	v_fma_f32 v37, s8, v220, v37
	v_fmac_f32_e32 v36, s8, v220
	v_pk_mul_f32 v[42:43], v[36:37], v[36:37]
	v_pk_mul_f32 v[44:45], v[34:35], v[34:35]
	v_fma_f32 v39, s8, v220, v39
	v_pk_mov_b32 v[46:47], v[44:45], v[42:43] op_sel:[1,0]
	v_mov_b32_e32 v45, v43
	v_fmac_f32_e32 v38, s8, v220
	v_fma_f32 v41, s8, v220, v41
	v_fmac_f32_e32 v40, s8, v220
	v_pk_add_f32 v[42:43], v[46:47], v[44:45]
	v_pk_mul_f32 v[44:45], v[40:41], v[40:41]
	v_pk_mul_f32 v[46:47], v[38:39], v[38:39]
	v_fmac_f32_e32 v98, s8, v220
	v_pk_mov_b32 v[48:49], v[46:47], v[44:45] op_sel:[1,0]
	v_mov_b32_e32 v47, v45
	v_fma_f32 v99, s8, v220, v99
	v_fmac_f32_e32 v92, s8, v220
	v_mul_f32_e32 v0, v98, v98
	v_pk_add_f32 v[44:45], v[48:49], v[46:47]
	v_fma_f32 v93, s8, v220, v93
	v_pk_fma_f32 v[46:47], v[98:99], v[98:99], v[0:1] op_sel_hi:[1,1,0]
	v_mul_f32_e32 v0, v92, v92
	v_pk_add_f32 v[42:43], v[42:43], v[42:43] op_sel_hi:[0,1]
	v_pk_add_f32 v[44:45], v[44:45], v[44:45] op_sel_hi:[0,1]
	v_pk_fma_f32 v[48:49], v[92:93], v[92:93], v[0:1] op_sel_hi:[1,1,0]
	v_fma_f32 v87, s8, v220, v87
	v_fmac_f32_e32 v86, s8, v220
	v_fma_f32 v95, s8, v220, v95
	v_fmac_f32_e32 v94, s8, v220
	v_mul_f32_e32 v46, v94, v94
	v_mul_f32_e32 v48, v95, v95
	v_mul_f32_e32 v42, v86, v86
	v_mul_f32_e32 v44, v87, v87
	v_pk_add_f32 v[46:47], v[46:47], v[48:49]
	v_pk_add_f32 v[42:43], v[42:43], v[44:45]
	s_nop 0
	v_pk_add_f32 v[42:43], v[46:47], v[42:43]
	s_nop 0
	v_add_f32_e32 v0, v42, v43
	v_mov_b32_e32 v42, v1
	s_nop 0
	v_add_f32_dpp v0, v0, v0 quad_perm:[1,0,3,2] row_mask:0xf bank_mask:0xf bound_ctrl:1
	s_nop 1
	v_add_f32_dpp v0, v0, v0 quad_perm:[2,3,0,1] row_mask:0xf bank_mask:0xf bound_ctrl:1
	s_nop 1
	v_add_f32_dpp v0, v0, v0 row_half_mirror row_mask:0xf bank_mask:0xf bound_ctrl:1
	s_nop 1
	v_add_f32_dpp v0, v0, v0 row_mirror row_mask:0xf bank_mask:0xf bound_ctrl:1
	s_nop 1
	v_mov_b32_dpp v42, v0 row_bcast:15 row_mask:0xa bank_mask:0xf
	v_add_f32_e32 v0, v0, v42
	v_mov_b32_e32 v42, v1
	s_nop 1
	v_mov_b32_dpp v42, v0 row_bcast:31 row_mask:0xc bank_mask:0xf
	v_add_f32_e32 v0, v0, v42
	s_nop 0
	v_readlane_b32 s8, v0, 63
	s_nop 1
	v_fma_f32 v0, s8, v221, v204
	v_rsq_f32_e32 v0, v0
	v_readlane_b32 s8, v255, 10
	v_readlane_b32 s9, v255, 11
	s_andn2_b64 vcc, exec, s[8:9]
	v_pk_mul_f32 v[34:35], v[34:35], v[0:1] op_sel_hi:[1,0]
	v_pk_mul_f32 v[36:37], v[36:37], v[0:1] op_sel_hi:[1,0]
	v_pk_fma_f32 v[46:47], v[2:3], v[34:35], v[6:7]
	v_pk_fma_f32 v[48:49], v[4:5], v[36:37], v[8:9]
	v_pk_mul_f32 v[34:35], v[38:39], v[0:1] op_sel_hi:[1,0]
	v_pk_mul_f32 v[36:37], v[40:41], v[0:1] op_sel_hi:[1,0]
	v_pk_fma_f32 v[42:43], v[10:11], v[34:35], v[14:15]
	v_pk_fma_f32 v[44:45], v[12:13], v[36:37], v[16:17]
	v_pk_mul_f32 v[34:35], v[98:99], v[0:1] op_sel_hi:[1,0]
	v_pk_mul_f32 v[36:37], v[92:93], v[0:1] op_sel_hi:[1,0]
	v_pk_mul_f32 v[38:39], v[94:95], v[0:1] op_sel_hi:[1,0]
	v_pk_mul_f32 v[40:41], v[86:87], v[0:1] op_sel_hi:[1,0]
	v_pk_fma_f32 v[36:37], v[20:21], v[36:37], v[24:25]
	v_pk_fma_f32 v[34:35], v[18:19], v[34:35], v[22:23]
	v_pk_fma_f32 v[40:41], v[28:29], v[40:41], v[32:33]
	v_pk_fma_f32 v[38:39], v[26:27], v[38:39], v[30:31]
	s_mov_b64 s[8:9], -1
	s_cbranch_vccnz .LBB0_1656
	s_mov_b32 s8, 0x7f807f81
	v_mul_hi_i32 v0, v72, s8
	v_lshrrev_b32_e32 v57, 31, v0
	v_ashrrev_i32_e32 v0, 11, v0
	v_add_u32_e32 v86, v0, v57
	v_mul_i32_i24_e32 v0, 0x1010, v86
	v_sub_u32_e32 v88, v72, v0
	v_ashrrev_i32_e32 v87, 31, v86
	v_readlane_b32 s16, v253, 0
	v_ashrrev_i32_e32 v89, 31, v88
	v_lshlrev_b64 v[86:87], 24, v[86:87]
	v_readlane_b32 s18, v253, 2
	v_readlane_b32 s19, v253, 3
	v_lshlrev_b64 v[88:89], 12, v[88:89]
	v_lshlrev_b32_e32 v0, 2, v149
	v_lshl_add_u64 v[86:87], s[18:19], 0, v[86:87]
	v_lshl_add_u64 v[86:87], v[86:87], 0, v[88:89]
	s_mov_b32 s8, 0xffff0000
	v_lshl_add_u64 v[86:87], v[86:87], 0, v[0:1]
	s_mov_b32 s9, -1
	v_lshl_add_u64 v[88:89], v[86:87], 0, s[8:9]
	v_add_co_u32_e32 v86, vcc, 0xffff0000, v86
	s_mov_b64 s[8:9], 0
	s_nop 0
	v_addc_co_u32_e32 v87, vcc, -1, v87, vcc
	v_readlane_b32 s17, v253, 1
	global_store_dwordx4 v[86:87], v[46:49], off
	global_store_dwordx4 v[88:89], v[42:45], off offset:1024
	global_store_dwordx4 v[88:89], v[34:37], off offset:2048
	global_store_dwordx4 v[88:89], v[38:41], off offset:3072

; __device__ __forceinline__ void ph_ln2(const Params& p, int l, LAS unsigned char* lds, const int wvid) {
;     ...
;     for (int r = gw; r < T; r += 4 * NGW, k += 4) {
;         u32x2 hv[4][4], av[4][4], cv[4][4]; bool on[4];
; #pragma unroll
;         for (int q = 0; q < 4; ++q) { const int rr = r + q * NGW; const int t = rr % LT; on[q] = rr < T && !(l == NLAYER - 1 && t < NMETA);
;             const int rc = rr < T ? rr : gw; const int s0 = __builtin_amdgcn_readlane(sl0, k + q), s1 = __builtin_amdgcn_readlane(sl1, k + q);
; #pragma unroll
;             for (int j = 0; j < 4; ++j) { hv[q][j] = *(const u32x2*)(HB + (size_t)rc * D + 4 * lane + 256 * j); av[q][j] = *(const u32x2*)(Y2 + (size_t)s0 * D + 4 * lane + 256 * j); cv[q][j] = *(const u32x2*)(Y2 + (size_t)s1 * D + 4 * lane + 256 * j); } }
.LBB0_1658:
	s_or_b64 exec, exec, s[10:11]
	s_add_i32 s46, s22, s82
	s_cmp_lt_i32 s46, 0x8080
	s_cbranch_scc0 .Lln2_drain2
	s_add_i32 s47, s46, s21
	s_cmp_lt_i32 s47, 0x8080
	s_cselect_b32 s48, s47, s40
	s_add_i32 s54, s62, 6
	v_readlane_b32 s50, v51, s54
	v_readlane_b32 s52, v148, s54
	s_ashr_i32 s49, s48, 31
	s_lshl_b64 s[48:49], s[48:49], 11
	s_ashr_i32 s51, s50, 31
	s_lshl_b64 s[50:51], s[50:51], 11
	s_ashr_i32 s53, s52, 31
	s_lshl_b64 s[52:53], s[52:53], 11
	v_lshl_add_u64 v[232:233], v[52:53], 0, s[48:49]
	v_lshl_add_u64 v[234:235], v[54:55], 0, s[50:51]
	v_lshl_add_u64 v[236:237], v[54:55], 0, s[52:53]
	global_load_dwordx2 v[106:107], v[232:233], off
	global_load_dwordx2 v[100:101], v[232:233], off offset:512
	global_load_dwordx2 v[92:93], v[232:233], off offset:1024
	global_load_dwordx2 v[88:89], v[232:233], off offset:1536
	global_load_dwordx2 v[110:111], v[234:235], off
	global_load_dwordx2 v[104:105], v[234:235], off offset:512
	global_load_dwordx2 v[96:97], v[234:235], off offset:1024
	global_load_dwordx2 v[90:91], v[234:235], off offset:1536
	global_load_dwordx2 v[108:109], v[236:237], off
	global_load_dwordx2 v[102:103], v[236:237], off offset:512
	global_load_dwordx2 v[94:95], v[236:237], off offset:1024
	global_load_dwordx2 v[86:87], v[236:237], off offset:1536
	s_branch .Lln2_next2

; __device__ __forceinline__ float bflo(unsigned w) { return __uint_as_float(w << 16); }
; __device__ __forceinline__ float bfhi(unsigned w) { return __uint_as_float(w & 0xFFFF0000u); }
; __device__ __forceinline__ void ph_ln2(const Params& p, int l, LAS unsigned char* lds, const int wvid) {
;     ...
;         for (int q = 0; q < 4; ++q) { const int rr = r + q * NGW; const int t = rr % LT; on[q] = rr < T && !(l == NLAYER - 1 && t < NMETA);
;             const int rc = rr < T ? rr : gw; const int s0 = __builtin_amdgcn_readlane(sl0, k + q), s1 = __builtin_amdgcn_readlane(sl1, k + q);
; #pragma unroll
;             for (int j = 0; j < 4; ++j) { hv[q][j] = *(const u32x2*)(HB + (size_t)rc * D + 4 * lane + 256 * j); av[q][j] = *(const u32x2*)(Y2 + (size_t)s0 * D + 4 * lane + 256 * j); cv[q][j] = *(const u32x2*)(Y2 + (size_t)s1 * D + 4 * lane + 256 * j); } }
; #pragma unroll
;         for (int q = 0; q < 4; ++q) { const int rr = r + q * NGW; if (!on[q]) continue; const int b = rr / LT, t = rr % LT;
;             f32x4 v[4];
; #pragma unroll
;             for (int j = 0; j < 4; ++j) { const u32x2 h = hv[q][j], a = av[q][j], c = cv[q][j];
;                 v[j][0] = ALPHA * bflo(h.x) + bflo(a.x) + bflo(c.x); v[j][1] = ALPHA * bfhi(h.x) + bfhi(a.x) + bfhi(c.x); v[j][2] = ALPHA * bflo(h.y) + bflo(a.y) + bflo(c.y); v[j][3] = ALPHA * bfhi(h.y) + bfhi(a.y) + bfhi(c.y); }
.Lln2_next2:
	v_add_u32_e32 v58, s32, v56
	s_add_i32 s60, s22, s32
	s_mul_hi_i32 s61, s60, 0x7f807f81
	s_lshr_b32 s55, s61, 31
	s_ashr_i32 s61, s61, 11
	s_add_i32 s61, s61, s55
	s_mul_i32 s61, s61, 0x1010
	s_sub_i32 s61, s60, s61
	s_cmp_gt_i32 s61, 15
	s_cselect_b64 s[6:7], -1, 0
	s_or_b64 s[6:7], s[6:7], s[42:43]
	s_cmp_lt_i32 s60, 0x8080
	s_cselect_b64 s[58:59], -1, 0
	s_and_b64 s[6:7], s[6:7], s[58:59]
	s_and_saveexec_b64 s[8:9], s[6:7]
	s_cbranch_execz .LBB0_1636
	s_waitcnt vmcnt(47)
	v_lshlrev_b32_e32 v34, 16, v80
	v_and_b32_e32 v35, 0xffff0000, v80
	s_waitcnt vmcnt(43)
	v_lshlrev_b32_e32 v36, 16, v84
	v_and_b32_e32 v37, 0xffff0000, v84
	v_pk_fma_f32 v[34:35], v[34:35], s[88:89], v[36:37] op_sel_hi:[1,0,1]
	s_waitcnt vmcnt(39)
	v_lshlrev_b32_e32 v36, 16, v82
	v_and_b32_e32 v37, 0xffff0000, v82
	v_pk_add_f32 v[34:35], v[34:35], v[36:37]
	v_lshlrev_b32_e32 v36, 16, v81
	v_and_b32_e32 v37, 0xffff0000, v81
	v_lshlrev_b32_e32 v38, 16, v85
	v_and_b32_e32 v39, 0xffff0000, v85
	v_pk_fma_f32 v[36:37], v[36:37], s[88:89], v[38:39] op_sel_hi:[1,0,1]
	v_lshlrev_b32_e32 v38, 16, v83
	v_and_b32_e32 v39, 0xffff0000, v83
	v_pk_add_f32 v[36:37], v[36:37], v[38:39]
	v_lshlrev_b32_e32 v38, 16, v74
	v_and_b32_e32 v39, 0xffff0000, v74
	v_lshlrev_b32_e32 v40, 16, v78
	v_and_b32_e32 v41, 0xffff0000, v78
	v_pk_fma_f32 v[38:39], v[38:39], s[88:89], v[40:41] op_sel_hi:[1,0,1]
	s_waitcnt vmcnt(38)
	v_lshlrev_b32_e32 v40, 16, v76
	v_and_b32_e32 v41, 0xffff0000, v76
	v_pk_add_f32 v[38:39], v[38:39], v[40:41]
	v_lshlrev_b32_e32 v40, 16, v75
	v_and_b32_e32 v41, 0xffff0000, v75
	v_lshlrev_b32_e32 v42, 16, v79
	v_and_b32_e32 v43, 0xffff0000, v79
	v_pk_fma_f32 v[40:41], v[40:41], s[88:89], v[42:43] op_sel_hi:[1,0,1]
	v_lshlrev_b32_e32 v42, 16, v77
	v_and_b32_e32 v43, 0xffff0000, v77
	v_pk_add_f32 v[40:41], v[40:41], v[42:43]
	v_lshlrev_b32_e32 v42, 16, v66
	v_and_b32_e32 v43, 0xffff0000, v66
	v_lshlrev_b32_e32 v44, 16, v70
	v_and_b32_e32 v45, 0xffff0000, v70
	v_pk_fma_f32 v[42:43], v[42:43], s[88:89], v[44:45] op_sel_hi:[1,0,1]
	s_waitcnt vmcnt(37)
	v_lshlrev_b32_e32 v44, 16, v68
	v_and_b32_e32 v45, 0xffff0000, v68
	v_pk_add_f32 v[72:73], v[42:43], v[44:45]
	v_lshlrev_b32_e32 v42, 16, v67
	v_and_b32_e32 v43, 0xffff0000, v67
	v_lshlrev_b32_e32 v44, 16, v71
	v_and_b32_e32 v45, 0xffff0000, v71
	v_pk_fma_f32 v[42:43], v[42:43], s[88:89], v[44:45] op_sel_hi:[1,0,1]
	v_lshlrev_b32_e32 v44, 16, v69
	v_and_b32_e32 v45, 0xffff0000, v69
	v_pk_add_f32 v[66:67], v[42:43], v[44:45]
	v_lshlrev_b32_e32 v42, 16, v62
	v_and_b32_e32 v43, 0xffff0000, v62
	v_lshlrev_b32_e32 v44, 16, v64
	v_and_b32_e32 v45, 0xffff0000, v64
	v_pk_fma_f32 v[42:43], v[42:43], s[88:89], v[44:45] op_sel_hi:[1,0,1]
	s_waitcnt vmcnt(36)
; __device__ __forceinline__ float frsq(float x) { return __builtin_amdgcn_rsqf(x); }
; __device__ __forceinline__ void ln_affine(f32x4 (&v)[4], const LnPar& q) {
;     float s = 0.f;
; #pragma unroll
;     for (int j = 0; j < 4; ++j) s += (v[j][0] + v[j][1]) + (v[j][2] + v[j][3]);
;     const float mean = wave_sum(s) * (1.f / D); float s2 = 0.f;
; #pragma unroll
;     for (int j = 0; j < 4; ++j) { v[j] = v[j] - mean; s2 += (v[j][0] * v[j][0] + v[j][1] * v[j][1]) + (v[j][2] * v[j][2] + v[j][3] * v[j][3]); }
;     const float rstd = frsq(wave_sum(s2) * (1.f / D) + 1e-5f);
; #pragma unroll
;     for (int j = 0; j < 4; ++j) v[j] = v[j] * rstd * q.g[j] + q.b[j];
; }
; __device__ __forceinline__ void ph_ln2(const Params& p, int l, LAS unsigned char* lds, const int wvid) {
;     ...
;             ln_affine(v, ln2);
;             if (l == NLAYER - 1) { float* o = p.out + ((size_t)b * SEQ + (t - NMETA)) * D;
; #pragma unroll
;                 for (int j = 0; j < 4; ++j) *(f32x4*)(o + 4 * lane + 256 * j) = v[j]; }
	v_lshlrev_b32_e32 v44, 16, v60
	v_and_b32_e32 v45, 0xffff0000, v60
	v_pk_add_f32 v[68:69], v[42:43], v[44:45]
	v_lshlrev_b32_e32 v42, 16, v63
	v_and_b32_e32 v43, 0xffff0000, v63
	v_lshlrev_b32_e32 v44, 16, v65
	v_and_b32_e32 v45, 0xffff0000, v65
	v_pk_fma_f32 v[42:43], v[42:43], s[88:89], v[44:45] op_sel_hi:[1,0,1]
	v_lshlrev_b32_e32 v44, 16, v61
	v_and_b32_e32 v45, 0xffff0000, v61
	v_pk_add_f32 v[60:61], v[42:43], v[44:45]
	v_mov_b32_e32 v42, v34
	v_mov_b32_e32 v43, v36
	v_mov_b32_e32 v44, v35
	v_mov_b32_e32 v45, v37
	v_pk_add_f32 v[42:43], v[42:43], v[44:45]
	v_mov_b32_e32 v44, v38
	v_mov_b32_e32 v45, v40
	v_mov_b32_e32 v46, v39
	v_mov_b32_e32 v47, v41
	v_pk_add_f32 v[44:45], v[44:45], v[46:47]
	v_add_f32_e32 v0, v42, v43
	v_pk_add_f32 v[44:45], v[44:45], v[44:45] op_sel:[0,1] op_sel_hi:[1,0]
	v_pk_add_f32 v[46:47], v[72:73], v[72:73] op_sel:[0,1] op_sel_hi:[1,0]
	v_pk_add_f32 v[48:49], v[66:67], v[66:67] op_sel:[0,1] op_sel_hi:[1,0]
	v_add_f32_e32 v42, 0, v0
	v_mov_b32_e32 v43, v68
	v_mov_b32_e32 v45, v69
	v_mov_b32_e32 v47, v60
	v_mov_b32_e32 v49, v61
	v_pk_add_f32 v[42:43], v[42:43], v[44:45]
	v_pk_add_f32 v[44:45], v[46:47], v[48:49]
	s_nop 0
	v_pk_add_f32 v[42:43], v[42:43], v[44:45]
	s_nop 0
	v_add_f32_e32 v0, v42, v43
	v_mov_b32_e32 v42, v1
	s_nop 0
	v_add_f32_dpp v0, v0, v0 quad_perm:[1,0,3,2] row_mask:0xf bank_mask:0xf bound_ctrl:1
	s_nop 1
	v_add_f32_dpp v0, v0, v0 quad_perm:[2,3,0,1] row_mask:0xf bank_mask:0xf bound_ctrl:1
	s_nop 1
	v_add_f32_dpp v0, v0, v0 row_half_mirror row_mask:0xf bank_mask:0xf bound_ctrl:1
	s_nop 1
	v_add_f32_dpp v0, v0, v0 row_mirror row_mask:0xf bank_mask:0xf bound_ctrl:1
	s_nop 1
	v_mov_b32_dpp v42, v0 row_bcast:15 row_mask:0xa bank_mask:0xf
	v_add_f32_e32 v0, v0, v42
	v_mov_b32_e32 v42, v1
	s_nop 1
	v_mov_b32_dpp v42, v0 row_bcast:31 row_mask:0xc bank_mask:0xf
	v_add_f32_e32 v0, v0, v42
	s_nop 0
	v_readlane_b32 s6, v0, 63
	s_nop 1
	v_fma_f32 v35, s6, v220, v35
	v_fmac_f32_e32 v34, s6, v220
	v_fma_f32 v37, s6, v220, v37
	v_fmac_f32_e32 v36, s6, v220
	v_pk_mul_f32 v[42:43], v[36:37], v[36:37]
	v_pk_mul_f32 v[44:45], v[34:35], v[34:35]
	v_fma_f32 v39, s6, v220, v39
	v_pk_mov_b32 v[46:47], v[44:45], v[42:43] op_sel:[1,0]
	v_mov_b32_e32 v45, v43
	v_fmac_f32_e32 v38, s6, v220
	v_fma_f32 v41, s6, v220, v41
	v_fmac_f32_e32 v40, s6, v220
	v_pk_add_f32 v[42:43], v[46:47], v[44:45]
	v_pk_mul_f32 v[44:45], v[40:41], v[40:41]
	v_pk_mul_f32 v[46:47], v[38:39], v[38:39]
	v_fmac_f32_e32 v72, s6, v220
	v_pk_mov_b32 v[48:49], v[46:47], v[44:45] op_sel:[1,0]
	v_mov_b32_e32 v47, v45
	v_fma_f32 v73, s6, v220, v73
	v_fmac_f32_e32 v66, s6, v220
	v_mul_f32_e32 v0, v72, v72
	v_pk_add_f32 v[44:45], v[48:49], v[46:47]
	v_fma_f32 v67, s6, v220, v67
	v_pk_fma_f32 v[46:47], v[72:73], v[72:73], v[0:1] op_sel_hi:[1,1,0]
	v_mul_f32_e32 v0, v66, v66
	v_pk_add_f32 v[42:43], v[42:43], v[42:43] op_sel_hi:[0,1]
	v_pk_add_f32 v[44:45], v[44:45], v[44:45] op_sel_hi:[0,1]
	v_pk_fma_f32 v[48:49], v[66:67], v[66:67], v[0:1] op_sel_hi:[1,1,0]
	v_fma_f32 v61, s6, v220, v61
	v_fmac_f32_e32 v60, s6, v220
	v_fma_f32 v69, s6, v220, v69
	v_fmac_f32_e32 v68, s6, v220
	v_mul_f32_e32 v46, v68, v68
	v_mul_f32_e32 v48, v69, v69
	v_mul_f32_e32 v42, v60, v60
	v_mul_f32_e32 v44, v61, v61
	v_pk_add_f32 v[46:47], v[46:47], v[48:49]
	v_pk_add_f32 v[42:43], v[42:43], v[44:45]
	s_nop 0
	v_pk_add_f32 v[42:43], v[46:47], v[42:43]
	s_nop 0
	v_add_f32_e32 v0, v42, v43
	v_mov_b32_e32 v42, v1
	s_nop 0
	v_add_f32_dpp v0, v0, v0 quad_perm:[1,0,3,2] row_mask:0xf bank_mask:0xf bound_ctrl:1
	s_nop 1
	v_add_f32_dpp v0, v0, v0 quad_perm:[2,3,0,1] row_mask:0xf bank_mask:0xf bound_ctrl:1
	s_nop 1
	v_add_f32_dpp v0, v0, v0 row_half_mirror row_mask:0xf bank_mask:0xf bound_ctrl:1
	s_nop 1
	v_add_f32_dpp v0, v0, v0 row_mirror row_mask:0xf bank_mask:0xf bound_ctrl:1
	s_nop 1
	v_mov_b32_dpp v42, v0 row_bcast:15 row_mask:0xa bank_mask:0xf
	v_add_f32_e32 v0, v0, v42
	v_mov_b32_e32 v42, v1
	s_nop 1
	v_mov_b32_dpp v42, v0 row_bcast:31 row_mask:0xc bank_mask:0xf
	v_add_f32_e32 v0, v0, v42
	s_nop 0
	v_readlane_b32 s6, v0, 63
	s_nop 1
	v_fma_f32 v0, s6, v221, v204
	v_rsq_f32_e32 v0, v0
	v_readlane_b32 s6, v255, 10
	v_readlane_b32 s7, v255, 11
	s_andn2_b64 vcc, exec, s[6:7]
	v_pk_mul_f32 v[34:35], v[34:35], v[0:1] op_sel_hi:[1,0]
	v_pk_mul_f32 v[36:37], v[36:37], v[0:1] op_sel_hi:[1,0]
	v_pk_fma_f32 v[46:47], v[2:3], v[34:35], v[6:7]
	v_pk_fma_f32 v[48:49], v[4:5], v[36:37], v[8:9]
	v_pk_mul_f32 v[34:35], v[38:39], v[0:1] op_sel_hi:[1,0]
	v_pk_mul_f32 v[36:37], v[40:41], v[0:1] op_sel_hi:[1,0]
	v_pk_fma_f32 v[42:43], v[10:11], v[34:35], v[14:15]
	v_pk_fma_f32 v[44:45], v[12:13], v[36:37], v[16:17]
	v_pk_mul_f32 v[34:35], v[72:73], v[0:1] op_sel_hi:[1,0]
	v_pk_mul_f32 v[36:37], v[66:67], v[0:1] op_sel_hi:[1,0]
	v_pk_mul_f32 v[38:39], v[68:69], v[0:1] op_sel_hi:[1,0]
	v_pk_mul_f32 v[40:41], v[60:61], v[0:1] op_sel_hi:[1,0]
	v_pk_fma_f32 v[36:37], v[20:21], v[36:37], v[24:25]
	v_pk_fma_f32 v[34:35], v[18:19], v[34:35], v[22:23]
	v_pk_fma_f32 v[40:41], v[28:29], v[40:41], v[32:33]
	v_pk_fma_f32 v[38:39], v[26:27], v[38:39], v[30:31]
	s_mov_b64 s[6:7], -1
	s_cbranch_vccnz .LBB0_1661
	s_mov_b32 s6, 0x7f807f81
	v_mul_hi_i32 v0, v58, s6
	v_lshrrev_b32_e32 v57, 31, v0
	v_ashrrev_i32_e32 v0, 11, v0
	v_add_u32_e32 v60, v0, v57
	v_mul_i32_i24_e32 v0, 0x1010, v60
	v_sub_u32_e32 v62, v58, v0
	v_ashrrev_i32_e32 v61, 31, v60
	v_readlane_b32 s16, v253, 0
	v_ashrrev_i32_e32 v63, 31, v62
	v_lshlrev_b64 v[60:61], 24, v[60:61]
	v_readlane_b32 s18, v253, 2
	v_readlane_b32 s19, v253, 3
	v_lshlrev_b64 v[62:63], 12, v[62:63]
	v_lshlrev_b32_e32 v0, 2, v149
	v_lshl_add_u64 v[60:61], s[18:19], 0, v[60:61]
	v_lshl_add_u64 v[60:61], v[60:61], 0, v[62:63]
	s_mov_b32 s6, 0xffff0000
	v_lshl_add_u64 v[60:61], v[60:61], 0, v[0:1]
	s_mov_b32 s7, -1
	v_lshl_add_u64 v[62:63], v[60:61], 0, s[6:7]
	v_add_co_u32_e32 v60, vcc, 0xffff0000, v60
	s_mov_b64 s[6:7], 0
	s_nop 0
	v_addc_co_u32_e32 v61, vcc, -1, v61, vcc
	v_readlane_b32 s17, v253, 1
	global_store_dwordx4 v[60:61], v[46:49], off
	global_store_dwordx4 v[62:63], v[42:45], off offset:1024
	global_store_dwordx4 v[62:63], v[34:37], off offset:2048
	global_store_dwordx4 v[62:63], v[38:41], off offset:3072
